# workgroup id remapped at entry to xcc + 8*ticket (arrival order per XCC) so every logical group always sits on one XCC and the group barriers always take the single-L2 path; plus spare-XCD layer-1 con
# baseline (speedup 1.0000x reference)
; #define KWS() ((unsigned char*)(GAS unsigned char*)karg()[20])
; __device__ __forceinline__ unsigned xb_xcc_id() { return (unsigned)__builtin_amdgcn_s_getreg((3 << 11) | 20) & 0xFu; }
; __global__ void __launch_bounds__(NWAVES * 64, 2) mk_fwd(Args args) {
;     ...
;     const int wave = __builtin_amdgcn_readfirstlane((int)threadIdx.x >> 6);
;     ...
;     const int G = gridDim.x, bid = blockIdx.x;
;     for (int u = threadIdx.x; u < (LDS_BYTES - MISC_OFF) / 4; u += NWAVES * 64) MISC[u] = 0u;
;     __syncthreads();
;     ...
;     XcdBarrier bar = xcd_barrier_post((unsigned*)(KWS() + WS_CTL) + CW_BAR, MISC + 40, wave);
;     if (threadIdx.x == 0) atomicOr(&bar.bar[LG_MASK(bid & 7)], 1u << bar.x);
_Z6mk_fwd4Args:
	s_mov_b64 s[78:79], s[0:1]
	s_load_dword s33, s[0:1], 0xb0
	s_add_u32 s0, s78, 0xb0
	s_addc_u32 s1, s79, 0
	s_mov_b32 s83, s2
	v_writelane_b32 v251, s0, 0
	v_readfirstlane_b32 s7, v0
	s_nop 0
	v_writelane_b32 v251, s1, 1
	s_movk_i32 s0, 0x100
	v_cmp_gt_u32_e32 vcc, s0, v0
	s_and_saveexec_b64 s[0:1], vcc
	v_lshl_add_u32 v1, v0, 2, 0
	v_add_u32_e32 v1, 0x27c00, v1
	v_mov_b32_e32 v2, 0
	ds_write_b32 v1, v2
	s_or_b64 exec, exec, s[0:1]
	s_mov_b64 s[0:1], s[78:79]
	s_waitcnt lgkmcnt(0)
	s_barrier
	s_cmp_lg_u32 s7, 0
	s_cbranch_scc1 .Lrm_wait
	s_load_dwordx2 s[98:99], s[78:79], 0xa0
	s_getreg_b32 s100, hwreg(HW_REG_XCC_ID, 0, 4)
	s_and_b32 s100, s100, 7
	s_lshl_b32 s101, s100, 6
	s_mov_b64 s[2:3], exec
	s_mov_b64 exec, 1
	v_mov_b32_e32 v252, s101
	v_mov_b32_e32 v253, 1
	s_waitcnt lgkmcnt(0)
	s_add_u32 s98, s98, 0x20000
	s_addc_u32 s99, s99, 0
	global_atomic_add v254, v252, v253, s[98:99] sc0
	s_waitcnt vmcnt(0)
	v_lshl_add_u32 v254, v254, 3, s100
	v_mov_b32_e32 v252, 0
	ds_write_b32 v252, v254
	s_waitcnt lgkmcnt(0)
	s_mov_b64 exec, s[2:3]
.Lrm_wait:
	s_barrier
	v_mov_b32_e32 v252, 0
	ds_read_b32 v252, v252
	s_waitcnt lgkmcnt(0)
	v_readfirstlane_b32 s83, v252
	s_nop 1
	s_barrier
	s_load_dwordx2 s[80:81], s[0:1], 0xa0
	s_getreg_b32 s0, hwreg(HW_REG_XCC_ID, 0, 4)
	s_waitcnt lgkmcnt(0)
	s_add_u32 s2, s80, 0x4000
	s_addc_u32 s3, s81, 0
	s_and_b32 s84, s0, 15
	v_writelane_b32 v251, s2, 2
	s_cmp_lt_u32 s7, 64
	s_cselect_b64 s[0:1], -1, 0
	v_writelane_b32 v251, s3, 3
	v_writelane_b32 v251, s0, 4
	s_cmp_gt_u32 s7, 63
	s_nop 0
	v_writelane_b32 v251, s1, 5
	s_cbranch_scc1 .LBB0_7
	v_mbcnt_lo_u32_b32 v1, -1, 0
	v_mbcnt_hi_u32_b32 v1, -1, v1
	s_nop 0
	v_cmp_eq_u32_e32 vcc, 0, v1
	s_and_saveexec_b64 s[0:1], vcc
	s_cbranch_execz .LBB0_6
	s_mov_b64 s[2:3], exec
	v_mbcnt_lo_u32_b32 v1, s2, 0
	v_mbcnt_hi_u32_b32 v1, s3, v1
	v_cmp_eq_u32_e32 vcc, 0, v1
	s_and_b64 s[4:5], exec, vcc
	s_mov_b64 exec, s[4:5]
	s_cbranch_execz .LBB0_6
	s_bcnt1_i32_b64 s2, s[2:3]
	s_lshl_b32 s4, s84, 8
	v_mov_b32_e32 v2, s2
	v_readlane_b32 s2, v251, 2
	v_mov_b32_e32 v1, s4
	v_readlane_b32 s3, v251, 3
	s_nop 4
	global_atomic_add v1, v2, s[2:3] offset:1024
